# GEMM accumulator zeroing with v_mov_b64 (64 instead of 128 moves per output tile)
# speedup vs baseline: 1.0072x; 1.0010x over previous
; template <class Epi, class Sched, bool ALIGN_EPI = false, bool SP2 = false>
; __device__ __forceinline__ void gemm_phase(PG8_LAS unsigned char* lds, const Gemm g, const Sched& S, const Epi& E) {
;     ...
;         for (int t = 0; t < nt; t += 2) {
;             if constexpr (Epi::MIDK) { if (t == (nt >> 1)) E.mid(acc, cur, wr, wc, fr, fq); }
;             const bool last = (t == nt - 2);
;             const char* a1 = cA + (size_t)(t + 1) * kstep;
;             const char* a2 = last ? nA : cA + (size_t)(t + 2) * kstep; const char* b2 = last ? nB : cB + (size_t)(t + 2) * kstep;
;             const char* a3 = a2 + kstep; const char* b3 = b2 + kstep;
;     ...
;         for (int a = 0; a < 2; ++a)
; #pragma unroll
;             for (int b = 0; b < 2; ++b)
; #pragma unroll
;                 for (int m = 0; m < 4; ++m)
; #pragma unroll
;                     for (int n = 0; n < 2; ++n) acc[a][b][m][n] = (f32x4){0.f, 0.f, 0.f, 0.f};
;         cur = nxt; cA = nA; cB = nB; ++ui;
.Lzk_1:
	s_add_u32 s2, s50, 0x80
	s_addc_u32 s3, s51, 0
	s_add_u32 s20, s48, 0x100
	s_addc_u32 s52, s49, 0
	s_mov_b32 s48, 0
	v_mov_b64_e32 v[42:43], 0
	v_mov_b64_e32 v[44:45], 0
	v_mov_b64_e32 v[46:47], 0
	v_mov_b64_e32 v[48:49], 0
	v_mov_b64_e32 v[58:59], 0
	v_mov_b64_e32 v[60:61], 0
	v_mov_b64_e32 v[62:63], 0
	v_mov_b64_e32 v[64:65], 0
	v_mov_b64_e32 v[74:75], 0
	v_mov_b64_e32 v[76:77], 0
	v_mov_b64_e32 v[78:79], 0
	v_mov_b64_e32 v[80:81], 0
	v_mov_b64_e32 v[90:91], 0
	v_mov_b64_e32 v[92:93], 0
	v_mov_b64_e32 v[94:95], 0
	v_mov_b64_e32 v[96:97], 0
	v_mov_b64_e32 v[98:99], 0
	v_mov_b64_e32 v[100:101], 0
	v_mov_b64_e32 v[102:103], 0
	v_mov_b64_e32 v[104:105], 0
	v_mov_b64_e32 v[114:115], 0
	v_mov_b64_e32 v[116:117], 0
	v_mov_b64_e32 v[118:119], 0
	v_mov_b64_e32 v[120:121], 0
	v_mov_b64_e32 v[130:131], 0
	v_mov_b64_e32 v[132:133], 0
	v_mov_b64_e32 v[134:135], 0
	v_mov_b64_e32 v[136:137], 0
	v_mov_b64_e32 v[146:147], 0
	v_mov_b64_e32 v[148:149], 0
	v_mov_b64_e32 v[150:151], 0
	v_mov_b64_e32 v[152:153], 0
	v_mov_b64_e32 v[106:107], 0
	v_mov_b64_e32 v[108:109], 0
	v_mov_b64_e32 v[110:111], 0
	v_mov_b64_e32 v[112:113], 0
	v_mov_b64_e32 v[122:123], 0
	v_mov_b64_e32 v[124:125], 0
	v_mov_b64_e32 v[126:127], 0
	v_mov_b64_e32 v[128:129], 0
	v_mov_b64_e32 v[138:139], 0
	v_mov_b64_e32 v[140:141], 0
	v_mov_b64_e32 v[142:143], 0
	v_mov_b64_e32 v[144:145], 0
	v_mov_b64_e32 v[154:155], 0
	v_mov_b64_e32 v[156:157], 0
	v_mov_b64_e32 v[158:159], 0
	v_mov_b64_e32 v[160:161], 0
	v_mov_b64_e32 v[86:87], 0
	v_mov_b64_e32 v[88:89], 0
	v_mov_b64_e32 v[82:83], 0
	v_mov_b64_e32 v[84:85], 0
	v_mov_b64_e32 v[70:71], 0
	v_mov_b64_e32 v[72:73], 0
	v_mov_b64_e32 v[66:67], 0
	v_mov_b64_e32 v[68:69], 0
	v_mov_b64_e32 v[54:55], 0
	v_mov_b64_e32 v[56:57], 0
	v_mov_b64_e32 v[50:51], 0
	v_mov_b64_e32 v[52:53], 0
	v_mov_b64_e32 v[38:39], 0
	v_mov_b64_e32 v[40:41], 0
	v_mov_b64_e32 v[34:35], 0
	v_mov_b64_e32 v[36:37], 0

;     __device__ __forceinline__ void mid(f32x4 (&acc)[2][2][4][2], const Unit& u, int wr, int wc, int fr, int fq) const {
;     ...
;                     for (int bj = 0; bj < 2; ++bj) { const size_t o = (size_t)(u.pm * BM + wr * 64 + fr + ai * HALF + (2 * mp + mm) * 16) * 2048 + u.pn * BM + wc * 64 + bj * 32 + 8 * fq;
;                         ga[mm][bj] = *(const uint2*)(gate + o); gm[mm][bj] = *(const uint2*)(gate + o + 1024); }
; template <class Epi, class Sched, bool ALIGN_EPI = false, bool SP2 = false>
; __device__ __forceinline__ void gemm_phase(PG8_LAS unsigned char* lds, const Gemm g, const Sched& S, const Epi& E) {
;     ...
;         for (int a = 0; a < 2; ++a)
; #pragma unroll
;             for (int b = 0; b < 2; ++b)
; #pragma unroll
;                 for (int m = 0; m < 4; ++m)
; #pragma unroll
;                     for (int n = 0; n < 2; ++n) acc[a][b][m][n] = (f32x4){0.f, 0.f, 0.f, 0.f};
;         cur = nxt; cA = nA; cB = nB; ++ui;
.Lzk_2:
	s_lshl_b32 s33, s69, 8
	v_add_u32_e32 v2, s33, v172
	v_ashrrev_i32_e32 v3, 31, v2
	s_lshl_b32 s0, s71, 8
	v_lshlrev_b64 v[6:7], 11, v[2:3]
	v_or_b32_e32 v2, 16, v2
	s_ashr_i32 s1, s0, 31
	v_ashrrev_i32_e32 v3, 31, v2
	v_lshl_add_u64 v[4:5], v[142:143], 0, s[0:1]
	v_lshlrev_b64 v[2:3], 11, v[2:3]
	v_lshl_add_u64 v[150:151], v[4:5], 0, v[2:3]
	v_or_b32_e32 v2, 32, v172
	v_add_u32_e32 v2, s33, v2
	v_ashrrev_i32_e32 v3, 31, v2
	v_lshl_add_u64 v[148:149], v[4:5], 0, v[6:7]
	v_lshlrev_b64 v[6:7], 11, v[2:3]
	v_or_b32_e32 v2, 16, v2
	v_ashrrev_i32_e32 v3, 31, v2
	v_lshlrev_b64 v[2:3], 11, v[2:3]
	v_lshl_add_u64 v[154:155], v[4:5], 0, v[2:3]
	v_add_u32_e32 v2, 0x80, v172
	v_add_u32_e32 v2, s33, v2
	v_ashrrev_i32_e32 v3, 31, v2
	v_lshl_add_u64 v[152:153], v[4:5], 0, v[6:7]
	v_lshlrev_b64 v[6:7], 11, v[2:3]
	v_or_b32_e32 v2, 16, v2
	v_ashrrev_i32_e32 v3, 31, v2
	v_lshlrev_b64 v[2:3], 11, v[2:3]
	v_lshl_add_u64 v[158:159], v[4:5], 0, v[2:3]
	v_add_u32_e32 v2, 0xa0, v172
	v_add_u32_e32 v2, s33, v2
	v_ashrrev_i32_e32 v3, 31, v2
	v_lshl_add_u64 v[156:157], v[4:5], 0, v[6:7]
	v_lshlrev_b64 v[6:7], 11, v[2:3]
	v_or_b32_e32 v2, 16, v2
	v_ashrrev_i32_e32 v3, 31, v2
	v_lshlrev_b64 v[2:3], 11, v[2:3]
	s_add_u32 s73, s40, 0x100
	v_lshl_add_u64 v[160:161], v[4:5], 0, v[6:7]
	v_lshl_add_u64 v[162:163], v[4:5], 0, v[2:3]
	s_addc_u32 s74, s41, 0
	v_lshl_add_u64 v[164:165], s[38:39], 0, v[144:145]
	v_lshl_add_u64 v[166:167], s[38:39], 0, v[146:147]
	s_mov_b32 s42, 0
	s_mov_b64 s[40:41], 0
	v_mov_b64_e32 v[10:11], 0
	v_mov_b64_e32 v[12:13], 0
	v_mov_b64_e32 v[14:15], 0
	v_mov_b64_e32 v[16:17], 0
	v_mov_b64_e32 v[26:27], 0
	v_mov_b64_e32 v[28:29], 0
	v_mov_b64_e32 v[30:31], 0
	v_mov_b64_e32 v[32:33], 0
	v_mov_b64_e32 v[42:43], 0
	v_mov_b64_e32 v[44:45], 0
	v_mov_b64_e32 v[46:47], 0
	v_mov_b64_e32 v[48:49], 0
	v_mov_b64_e32 v[58:59], 0
	v_mov_b64_e32 v[60:61], 0
	v_mov_b64_e32 v[62:63], 0
	v_mov_b64_e32 v[64:65], 0
	v_mov_b64_e32 v[66:67], 0
	v_mov_b64_e32 v[68:69], 0
	v_mov_b64_e32 v[70:71], 0
	v_mov_b64_e32 v[72:73], 0
	v_mov_b64_e32 v[82:83], 0
	v_mov_b64_e32 v[84:85], 0
	v_mov_b64_e32 v[86:87], 0
	v_mov_b64_e32 v[88:89], 0
	v_mov_b64_e32 v[98:99], 0
	v_mov_b64_e32 v[100:101], 0
	v_mov_b64_e32 v[102:103], 0
	v_mov_b64_e32 v[104:105], 0
	v_mov_b64_e32 v[114:115], 0
	v_mov_b64_e32 v[116:117], 0
	v_mov_b64_e32 v[118:119], 0
	v_mov_b64_e32 v[120:121], 0
	v_mov_b64_e32 v[74:75], 0
	v_mov_b64_e32 v[76:77], 0
	v_mov_b64_e32 v[78:79], 0
	v_mov_b64_e32 v[80:81], 0
	v_mov_b64_e32 v[90:91], 0
	v_mov_b64_e32 v[92:93], 0
	v_mov_b64_e32 v[94:95], 0
	v_mov_b64_e32 v[96:97], 0
	v_mov_b64_e32 v[106:107], 0
	v_mov_b64_e32 v[108:109], 0
	v_mov_b64_e32 v[110:111], 0
	v_mov_b64_e32 v[112:113], 0
	v_mov_b64_e32 v[122:123], 0
	v_mov_b64_e32 v[124:125], 0
	v_mov_b64_e32 v[126:127], 0
	v_mov_b64_e32 v[128:129], 0
	v_mov_b64_e32 v[54:55], 0
	v_mov_b64_e32 v[56:57], 0
	v_mov_b64_e32 v[50:51], 0
	v_mov_b64_e32 v[52:53], 0
	v_mov_b64_e32 v[38:39], 0
	v_mov_b64_e32 v[40:41], 0
	v_mov_b64_e32 v[34:35], 0
	v_mov_b64_e32 v[36:37], 0
	v_mov_b64_e32 v[22:23], 0
	v_mov_b64_e32 v[24:25], 0
	v_mov_b64_e32 v[18:19], 0
	v_mov_b64_e32 v[20:21], 0
	v_mov_b64_e32 v[6:7], 0
	v_mov_b64_e32 v[8:9], 0
	v_mov_b64_e32 v[2:3], 0
	v_mov_b64_e32 v[4:5], 0
	s_cmp_lg_u32 s56, s42
	s_cbranch_scc1 .LBB0_984
	s_branch .LBB0_983

; template <class Epi, class Sched, bool ALIGN_EPI = false, bool SP2 = false>
; __device__ __forceinline__ void gemm_phase(PG8_LAS unsigned char* lds, const Gemm g, const Sched& S, const Epi& E) {
;     ...
;         for (int a = 0; a < 2; ++a)
; #pragma unroll
;             for (int b = 0; b < 2; ++b)
; #pragma unroll
;                 for (int m = 0; m < 4; ++m)
; #pragma unroll
;                     for (int n = 0; n < 2; ++n) acc[a][b][m][n] = (f32x4){0.f, 0.f, 0.f, 0.f};
;         cur = nxt; cA = nA; cB = nB; ++ui;
.Lzk_3:
	s_add_u32 s56, s56, 0x80
	s_addc_u32 s57, s57, 0
	s_add_u32 s93, s58, 0x100
	s_addc_u32 s94, s59, 0
	s_mov_b32 s58, 0
	v_mov_b64_e32 v[6:7], 0
	v_mov_b64_e32 v[8:9], 0
	v_mov_b64_e32 v[14:15], 0
	v_mov_b64_e32 v[16:17], 0
	v_mov_b64_e32 v[26:27], 0
	v_mov_b64_e32 v[28:29], 0
	v_mov_b64_e32 v[30:31], 0
	v_mov_b64_e32 v[32:33], 0
	v_mov_b64_e32 v[42:43], 0
	v_mov_b64_e32 v[44:45], 0
	v_mov_b64_e32 v[46:47], 0
	v_mov_b64_e32 v[48:49], 0
	v_mov_b64_e32 v[86:87], 0
	v_mov_b64_e32 v[88:89], 0
	v_mov_b64_e32 v[82:83], 0
	v_mov_b64_e32 v[84:85], 0
	v_mov_b64_e32 v[78:79], 0
	v_mov_b64_e32 v[80:81], 0
	v_mov_b64_e32 v[74:75], 0
	v_mov_b64_e32 v[76:77], 0
	v_mov_b64_e32 v[94:95], 0
	v_mov_b64_e32 v[96:97], 0
	v_mov_b64_e32 v[90:91], 0
	v_mov_b64_e32 v[92:93], 0
	v_mov_b64_e32 v[54:55], 0
	v_mov_b64_e32 v[56:57], 0
	v_mov_b64_e32 v[50:51], 0
	v_mov_b64_e32 v[52:53], 0
	v_mov_b64_e32 v[114:115], 0
	v_mov_b64_e32 v[116:117], 0
	v_mov_b64_e32 v[118:119], 0
	v_mov_b64_e32 v[120:121], 0
	v_mov_b64_e32 v[102:103], 0
	v_mov_b64_e32 v[104:105], 0
	v_mov_b64_e32 v[98:99], 0
	v_mov_b64_e32 v[100:101], 0
	v_mov_b64_e32 v[110:111], 0
	v_mov_b64_e32 v[112:113], 0
	v_mov_b64_e32 v[106:107], 0
	v_mov_b64_e32 v[108:109], 0
	v_mov_b64_e32 v[62:63], 0
	v_mov_b64_e32 v[64:65], 0
	v_mov_b64_e32 v[58:59], 0
	v_mov_b64_e32 v[60:61], 0
	v_mov_b64_e32 v[122:123], 0
	v_mov_b64_e32 v[124:125], 0
	v_mov_b64_e32 v[126:127], 0
	v_mov_b64_e32 v[128:129], 0
	v_mov_b64_e32 v[66:67], 0
	v_mov_b64_e32 v[68:69], 0
	v_mov_b64_e32 v[70:71], 0
	v_mov_b64_e32 v[72:73], 0
	v_mov_b64_e32 v[38:39], 0
	v_mov_b64_e32 v[40:41], 0
	v_mov_b64_e32 v[34:35], 0
	v_mov_b64_e32 v[36:37], 0
	v_mov_b64_e32 v[22:23], 0
	v_mov_b64_e32 v[24:25], 0
	v_mov_b64_e32 v[18:19], 0
	v_mov_b64_e32 v[20:21], 0
	v_mov_b64_e32 v[10:11], 0
	v_mov_b64_e32 v[12:13], 0
	v_mov_b64_e32 v[2:3], 0
	v_mov_b64_e32 v[4:5], 0

; template <class Epi, class Sched, bool ALIGN_EPI = false, bool SP2 = false>
; __device__ __forceinline__ void gemm_phase(PG8_LAS unsigned char* lds, const Gemm g, const Sched& S, const Epi& E) {
;     ...
;         for (int a = 0; a < 2; ++a)
; #pragma unroll
;             for (int b = 0; b < 2; ++b)
; #pragma unroll
;                 for (int m = 0; m < 4; ++m)
; #pragma unroll
;                     for (int n = 0; n < 2; ++n) acc[a][b][m][n] = (f32x4){0.f, 0.f, 0.f, 0.f};
;         cur = nxt; cA = nA; cB = nB; ++ui;
.Lzk_4:
	s_add_u32 s30, s30, 0x80
	s_addc_u32 s31, s31, 0
	s_add_u32 s58, s34, 0x100
	s_addc_u32 s59, s35, 0
	s_mov_b32 s34, 0
	v_mov_b64_e32 v[6:7], 0
	v_mov_b64_e32 v[8:9], 0
	v_mov_b64_e32 v[14:15], 0
	v_mov_b64_e32 v[16:17], 0
	v_mov_b64_e32 v[26:27], 0
	v_mov_b64_e32 v[28:29], 0
	v_mov_b64_e32 v[30:31], 0
	v_mov_b64_e32 v[32:33], 0
	v_mov_b64_e32 v[42:43], 0
	v_mov_b64_e32 v[44:45], 0
	v_mov_b64_e32 v[46:47], 0
	v_mov_b64_e32 v[48:49], 0
	v_mov_b64_e32 v[58:59], 0
	v_mov_b64_e32 v[60:61], 0
	v_mov_b64_e32 v[62:63], 0
	v_mov_b64_e32 v[64:65], 0
	v_mov_b64_e32 v[66:67], 0
	v_mov_b64_e32 v[68:69], 0
	v_mov_b64_e32 v[70:71], 0
	v_mov_b64_e32 v[72:73], 0
	v_mov_b64_e32 v[82:83], 0
	v_mov_b64_e32 v[84:85], 0
	v_mov_b64_e32 v[86:87], 0
	v_mov_b64_e32 v[88:89], 0
	v_mov_b64_e32 v[98:99], 0
	v_mov_b64_e32 v[100:101], 0
	v_mov_b64_e32 v[102:103], 0
	v_mov_b64_e32 v[104:105], 0
	v_mov_b64_e32 v[114:115], 0
	v_mov_b64_e32 v[116:117], 0
	v_mov_b64_e32 v[118:119], 0
	v_mov_b64_e32 v[120:121], 0
	v_mov_b64_e32 v[74:75], 0
	v_mov_b64_e32 v[76:77], 0
	v_mov_b64_e32 v[78:79], 0
	v_mov_b64_e32 v[80:81], 0
	v_mov_b64_e32 v[90:91], 0
	v_mov_b64_e32 v[92:93], 0
	v_mov_b64_e32 v[94:95], 0
	v_mov_b64_e32 v[96:97], 0
	v_mov_b64_e32 v[106:107], 0
	v_mov_b64_e32 v[108:109], 0
	v_mov_b64_e32 v[110:111], 0
	v_mov_b64_e32 v[112:113], 0
	v_mov_b64_e32 v[122:123], 0
	v_mov_b64_e32 v[124:125], 0
	v_mov_b64_e32 v[126:127], 0
	v_mov_b64_e32 v[128:129], 0
	v_mov_b64_e32 v[54:55], 0
	v_mov_b64_e32 v[56:57], 0
	v_mov_b64_e32 v[50:51], 0
	v_mov_b64_e32 v[52:53], 0
	v_mov_b64_e32 v[38:39], 0
	v_mov_b64_e32 v[40:41], 0
	v_mov_b64_e32 v[34:35], 0
	v_mov_b64_e32 v[36:37], 0
	v_mov_b64_e32 v[22:23], 0
	v_mov_b64_e32 v[24:25], 0
	v_mov_b64_e32 v[18:19], 0
	v_mov_b64_e32 v[20:21], 0
	v_mov_b64_e32 v[10:11], 0
	v_mov_b64_e32 v[12:13], 0
	v_mov_b64_e32 v[2:3], 0
	v_mov_b64_e32 v[4:5], 0

; template <class Epi, class Sched, bool ALIGN_EPI = false, bool SP2 = false>
; __device__ __forceinline__ void gemm_phase(PG8_LAS unsigned char* lds, const Gemm g, const Sched& S, const Epi& E) {
;     ...
;         for (int a = 0; a < 2; ++a)
; #pragma unroll
;             for (int b = 0; b < 2; ++b)
; #pragma unroll
;                 for (int m = 0; m < 4; ++m)
; #pragma unroll
;                     for (int n = 0; n < 2; ++n) acc[a][b][m][n] = (f32x4){0.f, 0.f, 0.f, 0.f};
;         cur = nxt; cA = nA; cB = nB; ++ui;
.Lzk_6:
	s_add_u32 s46, s46, 0x80
	s_addc_u32 s47, s47, 0
	s_add_u32 s80, s48, 0x100
	s_addc_u32 s81, s49, 0
	s_mov_b32 s48, 0
	v_mov_b64_e32 v[42:43], 0
	v_mov_b64_e32 v[44:45], 0
	v_mov_b64_e32 v[46:47], 0
	v_mov_b64_e32 v[48:49], 0
	v_mov_b64_e32 v[58:59], 0
	v_mov_b64_e32 v[60:61], 0
	v_mov_b64_e32 v[62:63], 0
	v_mov_b64_e32 v[64:65], 0
	v_mov_b64_e32 v[74:75], 0
	v_mov_b64_e32 v[76:77], 0
	v_mov_b64_e32 v[78:79], 0
	v_mov_b64_e32 v[80:81], 0
	v_mov_b64_e32 v[90:91], 0
	v_mov_b64_e32 v[92:93], 0
	v_mov_b64_e32 v[94:95], 0
	v_mov_b64_e32 v[96:97], 0
	v_mov_b64_e32 v[98:99], 0
	v_mov_b64_e32 v[100:101], 0
	v_mov_b64_e32 v[102:103], 0
	v_mov_b64_e32 v[104:105], 0
	v_mov_b64_e32 v[114:115], 0
	v_mov_b64_e32 v[116:117], 0
	v_mov_b64_e32 v[118:119], 0
	v_mov_b64_e32 v[120:121], 0
	v_mov_b64_e32 v[130:131], 0
	v_mov_b64_e32 v[132:133], 0
	v_mov_b64_e32 v[134:135], 0
	v_mov_b64_e32 v[136:137], 0
	v_mov_b64_e32 v[146:147], 0
	v_mov_b64_e32 v[148:149], 0
	v_mov_b64_e32 v[150:151], 0
	v_mov_b64_e32 v[152:153], 0
	v_mov_b64_e32 v[106:107], 0
	v_mov_b64_e32 v[108:109], 0
	v_mov_b64_e32 v[110:111], 0
	v_mov_b64_e32 v[112:113], 0
	v_mov_b64_e32 v[122:123], 0
	v_mov_b64_e32 v[124:125], 0
	v_mov_b64_e32 v[126:127], 0
	v_mov_b64_e32 v[128:129], 0
	v_mov_b64_e32 v[138:139], 0
	v_mov_b64_e32 v[140:141], 0
	v_mov_b64_e32 v[142:143], 0
	v_mov_b64_e32 v[144:145], 0
	v_mov_b64_e32 v[154:155], 0
	v_mov_b64_e32 v[156:157], 0
	v_mov_b64_e32 v[158:159], 0
	v_mov_b64_e32 v[160:161], 0
	v_mov_b64_e32 v[86:87], 0
	v_mov_b64_e32 v[88:89], 0
	v_mov_b64_e32 v[82:83], 0
	v_mov_b64_e32 v[84:85], 0
	v_mov_b64_e32 v[70:71], 0
	v_mov_b64_e32 v[72:73], 0
	v_mov_b64_e32 v[66:67], 0
	v_mov_b64_e32 v[68:69], 0
	v_mov_b64_e32 v[54:55], 0
	v_mov_b64_e32 v[56:57], 0
	v_mov_b64_e32 v[50:51], 0
	v_mov_b64_e32 v[52:53], 0
	v_mov_b64_e32 v[38:39], 0
	v_mov_b64_e32 v[40:41], 0
	v_mov_b64_e32 v[34:35], 0
	v_mov_b64_e32 v[36:37], 0

; template <class Epi, class Sched, bool ALIGN_EPI = false, bool SP2 = false>
; __device__ __forceinline__ void gemm_phase(PG8_LAS unsigned char* lds, const Gemm g, const Sched& S, const Epi& E) {
;     ...
; #pragma unroll
;         for (int a = 0; a < 2; ++a)
; #pragma unroll
;             for (int b = 0; b < 2; ++b)
; #pragma unroll
;                 for (int m = 0; m < 4; ++m)
; #pragma unroll
;                     for (int n = 0; n < 2; ++n) acc[a][b][m][n] = (f32x4){0.f, 0.f, 0.f, 0.f};
;         cur = nxt; cA = nA; cB = nB; ++ui;
.Lzk_7:
	s_add_u32 s2, s80, 0x80
	s_addc_u32 s3, s81, 0
	s_add_u32 s57, s78, 0x100
	s_addc_u32 s82, s79, 0
	s_mov_b32 s78, 0
	v_mov_b64_e32 v[40:41], 0
	v_mov_b64_e32 v[42:43], 0
	v_mov_b64_e32 v[44:45], 0
	v_mov_b64_e32 v[46:47], 0
	v_mov_b64_e32 v[56:57], 0
	v_mov_b64_e32 v[58:59], 0
	v_mov_b64_e32 v[60:61], 0
	v_mov_b64_e32 v[62:63], 0
	v_mov_b64_e32 v[72:73], 0
	v_mov_b64_e32 v[74:75], 0
	v_mov_b64_e32 v[76:77], 0
	v_mov_b64_e32 v[78:79], 0
	v_mov_b64_e32 v[88:89], 0
	v_mov_b64_e32 v[90:91], 0
	v_mov_b64_e32 v[92:93], 0
	v_mov_b64_e32 v[94:95], 0
	v_mov_b64_e32 v[96:97], 0
	v_mov_b64_e32 v[98:99], 0
	v_mov_b64_e32 v[100:101], 0
	v_mov_b64_e32 v[102:103], 0
	v_mov_b64_e32 v[120:121], 0
	v_mov_b64_e32 v[122:123], 0
	v_mov_b64_e32 v[124:125], 0
	v_mov_b64_e32 v[126:127], 0
	v_mov_b64_e32 v[128:129], 0
	v_mov_b64_e32 v[130:131], 0
	v_mov_b64_e32 v[132:133], 0
	v_mov_b64_e32 v[134:135], 0
	v_mov_b64_e32 v[144:145], 0
	v_mov_b64_e32 v[146:147], 0
	v_mov_b64_e32 v[148:149], 0
	v_mov_b64_e32 v[150:151], 0
	v_mov_b64_e32 v[112:113], 0
	v_mov_b64_e32 v[114:115], 0
	v_mov_b64_e32 v[116:117], 0
	v_mov_b64_e32 v[118:119], 0
	v_mov_b64_e32 v[104:105], 0
	v_mov_b64_e32 v[106:107], 0
	v_mov_b64_e32 v[108:109], 0
	v_mov_b64_e32 v[110:111], 0
	v_mov_b64_e32 v[136:137], 0
	v_mov_b64_e32 v[138:139], 0
	v_mov_b64_e32 v[140:141], 0
	v_mov_b64_e32 v[142:143], 0
	v_mov_b64_e32 v[160:161], 0
	v_mov_b64_e32 v[162:163], 0
	v_mov_b64_e32 v[164:165], 0
	v_mov_b64_e32 v[166:167], 0
	v_mov_b64_e32 v[84:85], 0
	v_mov_b64_e32 v[86:87], 0
	v_mov_b64_e32 v[80:81], 0
	v_mov_b64_e32 v[82:83], 0
	v_mov_b64_e32 v[68:69], 0
	v_mov_b64_e32 v[70:71], 0
	v_mov_b64_e32 v[64:65], 0
	v_mov_b64_e32 v[66:67], 0
	v_mov_b64_e32 v[52:53], 0
	v_mov_b64_e32 v[54:55], 0
	v_mov_b64_e32 v[48:49], 0
	v_mov_b64_e32 v[50:51], 0
	v_mov_b64_e32 v[36:37], 0
	v_mov_b64_e32 v[38:39], 0
	v_mov_b64_e32 v[32:33], 0
	v_mov_b64_e32 v[34:35], 0
